# lever 4: one static priority raise for waves 4-7 (one wave of each SIMD pair) over the NA unit loop, reset at loop exit
# speedup vs baseline: 1.0061x; 1.0061x over previous
; #define LAS __attribute__((address_space(3)))
; __device__ __forceinline__ void na_fast_unit(int unit, const bf16_t* P, const float* rpb, bf16_t* AO, LAS unsigned char* lds) {
;     const int tid = threadIdx.x, lane = tid & 63, wv = __builtin_amdgcn_readfirstlane(tid >> 6);
;     const int cq = wv & 3, kh = wv >> 2;
;     const int r = unit & 63, h = (unit >> 6) & 7, b = unit >> 9;
;     const int l15 = lane & 15, q = lane >> 4, trq = l15 >> 2, trp = lane & 3;
;     const int rstart = min(max(r - 4, 0), 56);
;     const int col = 16 * cq + l15, cstart = min(max(col - 8, 0), 48);
;     const int ct0 = min(max(cq - 1, 0), 1);
;     const float scale = 0.08838834764831845f;
; __global__ void __launch_bounds__(512, 2) mk_fwd(Args a) {
;     ...
;         unsigned* qctr = (unsigned*)(ws + WS_CTL) + 8192 + 64 * rep;
;         for (;;) {
;             __syncthreads();
;             if (tid == 0) *(volatile LAS unsigned*)(lds + LDS_BARW + 32) = atomicAdd(qctr, 1u);
;             __syncthreads();
;             const unsigned u = *(volatile LAS unsigned*)(lds + LDS_BARW + 32);
;             if (u >= (unsigned)(NB * 8 * 64)) break;
;             na_fast_unit((int)u, Pb, a.in[I_RPB], AO, lds);
.LBB0_1206:
	v_or_b32_e32 v3, 0x600, v0
	s_add_u32 s8, s94, 0x8000
	v_and_b32_e32 v2, 0x78, v181
	v_or_b32_e32 v104, 64, v168
	v_lshrrev_b32_e32 v105, 4, v3
	v_readlane_b32 s6, v255, 3
	s_addc_u32 s9, s95, 0
	v_bfe_u32 v106, v3, 4, 6
	v_mul_u32_u24_e32 v107, 0x110, v168
	v_mul_u32_u24_e32 v108, 0x110, v170
	v_mul_u32_u24_e32 v109, 0x120, v104
	v_mul_u32_u24_e32 v110, 0x110, v105
	v_mul_u32_u24_e32 v111, 0x120, v105
	s_add_i32 s2, 0, 0x11800
	s_add_i32 s3, 0, 0x1a000
	v_lshlrev_b32_e32 v114, 11, v86
	v_lshl_add_u32 v115, v1, 2, 0
	v_lshlrev_b32_e32 v86, 1, v1
	v_readlane_b32 s7, v255, 4
	v_mov_b32_e32 v3, 0x200
	s_add_i32 s45, 0, 0x23fe0
	v_lshlrev_b32_e32 v92, 1, v2
	v_mbcnt_lo_u32_b32 v2, -1, 0
	v_cmp_eq_u32_e64 s[4:5], 0, v0
	s_movk_i32 s13, 0x110
	v_add_u32_e32 v112, s2, v176
	v_add_u32_e32 v113, s3, v178
	v_add_u32_e32 v116, v115, v114
	v_lshl_add_u64 v[88:89], s[6:7], 0, v[86:87]
	v_lshl_or_b32 v117, v169, 9, v3
	v_lshlrev_b32_e32 v118, 9, v180
	v_lshlrev_b32_e32 v119, 9, v179
	v_add_u32_e32 v120, 0, v176
	v_add_u32_e32 v121, 0, v178
	v_add_u32_e32 v122, s2, v177
	v_add_u32_e32 v123, s3, v177
	v_lshl_add_u32 v124, v169, 2, 0
	v_mov_b32_e32 v125, s45
	s_movk_i32 s46, 0x3200
	s_mov_b64 s[10:11], 0x1400
	s_movk_i32 s47, 0x1000
	v_add_u32_e32 v126, v174, v107
	v_add_u32_e32 v127, v174, v171
	v_add_u32_e32 v128, v174, v108
	v_add_u32_e32 v129, v174, v172
	v_add_u32_e32 v130, v174, v109
	v_add_u32_e32 v131, v174, v110
	v_add_u32_e32 v132, v174, v111
	s_mov_b32 s12, 0x3db504f3
	v_lshlrev_b32_e32 v90, 1, v175
	v_mbcnt_hi_u32_b32 v133, -1, v2
	s_and_saveexec_b64 s[2:3], s[4:5]
	v_mov_b32_e32 v3, 1
	global_atomic_add v253, v87, v3, s[8:9] sc0
	s_waitcnt vmcnt(0)
	s_mov_b64 exec, s[2:3]
	v_readfirstlane_b32 s2, v0
	s_cmpk_lt_u32 s2, 0x100
	s_cbranch_scc1 .Lna_prio_skip
	s_setprio 1
.Lna_prio_skip:
	s_branch .LBB0_1209
.LBB0_1207:
	s_mov_b64 s[2:3], 0
	s_barrier

; #define LAS __attribute__((address_space(3)))
; __device__ __forceinline__ unsigned xb_add(unsigned* p, unsigned v) { return __hip_atomic_fetch_add(p, v, __ATOMIC_RELAXED, __HIP_MEMORY_SCOPE_AGENT); }
; __device__ __forceinline__ void phase_prologue(const Args& a, LAS unsigned char* lds) {
;     ...
;     unsigned* cq_head = (unsigned*)(a.ws + WS_CTL) + 8192 + 768;
;     volatile LAS int* qs = (volatile LAS int*)(lds + 128 * 129 * 4);
;     int pend = 0, it = 0;
;     if (tid == 0) { qs[0] = (int)xb_add(cq_head, 1u); pend = (int)xb_add(cq_head, 1u); }
;     __syncthreads();
.Lcva_entry:
	s_setprio 0
	s_waitcnt vmcnt(0) lgkmcnt(0)
	s_barrier
	v_mov_b32_e32 v119, 1
	v_mov_b32_e32 v120, 0x9000
	v_mov_b32_e32 v121, 0x9100
	v_mov_b32_e32 v122, 0
	v_mov_b32_e32 v125, 0x10200
	s_mov_b32 s25, 0
	v_cmp_eq_u32_e32 vcc, 0, v0
	s_and_saveexec_b64 s[34:35], vcc
	s_cbranch_execz .Lcva_f0
	global_atomic_add v124, v121, v122, s[94:95] sc0
	s_waitcnt vmcnt(0)
	ds_write_b32 v125, v124 offset:4
